# speedup vs baseline: 1.0080x; 1.0056x over previous
.LBB0_56:
	s_or_b64 exec, exec, s[8:9]
	s_mov_b32 s10, 0xaaaaaaaa
	s_mov_b32 s11, 0xaaaaaaaa
	s_waitcnt vmcnt(0)
	v_cvt_pk_f16_f32 v14, v14, v15
	v_cvt_pk_f16_f32 v15, v16, v17
	v_cvt_pk_f16_f32 v2, v2, v3
	v_cvt_pk_f16_f32 v3, v4, v5
	v_cvt_pk_f16_f32 v18, v18, v19
	v_cvt_pk_f16_f32 v19, v20, v21
	v_cvt_pk_f16_f32 v6, v6, v7
	v_cvt_pk_f16_f32 v7, v8, v9
	v_cvt_pk_f16_f32 v22, v22, v23
	v_cvt_pk_f16_f32 v23, v24, v25
	v_cvt_pk_f16_f32 v10, v10, v11
	v_cvt_pk_f16_f32 v11, v12, v13
	v_cndmask_b32_e64 v4, v2, v14, s[10:11]
	v_cndmask_b32_e64 v5, v3, v15, s[10:11]
	v_lshlrev_b32_e32 v8, 3, v30
	v_lshlrev_b32_e32 v9, 3, v32
	v_mov_b32_dpp v16, v4 quad_perm:[1,0,3,2] row_mask:0xf bank_mask:0xf
	v_mov_b32_dpp v17, v5 quad_perm:[1,0,3,2] row_mask:0xf bank_mask:0xf
	v_add_u32_e32 v9, -8, v9
	v_cndmask_b32_e64 v44, v14, v16, s[10:11]
	v_cndmask_b32_e64 v45, v15, v17, s[10:11]
	v_cndmask_b32_e64 v46, v16, v2, s[10:11]
	v_cndmask_b32_e64 v47, v17, v3, s[10:11]
	v_cndmask_b32_e64 v8, v8, v9, s[10:11]
	global_store_dwordx4 v8, v[44:47], s[4:5] sc1
	v_cndmask_b32_e64 v4, v6, v18, s[10:11]
	v_cndmask_b32_e64 v5, v7, v19, s[10:11]
	v_lshlrev_b32_e32 v8, 3, v38
	v_lshlrev_b32_e32 v9, 3, v34
	v_mov_b32_dpp v16, v4 quad_perm:[1,0,3,2] row_mask:0xf bank_mask:0xf
	v_mov_b32_dpp v17, v5 quad_perm:[1,0,3,2] row_mask:0xf bank_mask:0xf
	v_add_u32_e32 v9, -8, v9
	v_cndmask_b32_e64 v44, v18, v16, s[10:11]
	v_cndmask_b32_e64 v45, v19, v17, s[10:11]
	v_cndmask_b32_e64 v46, v16, v6, s[10:11]
	v_cndmask_b32_e64 v47, v17, v7, s[10:11]
	v_cndmask_b32_e64 v8, v8, v9, s[10:11]
	global_store_dwordx4 v8, v[44:47], s[4:5] sc1
	v_cndmask_b32_e64 v4, v10, v22, s[10:11]
	v_cndmask_b32_e64 v5, v11, v23, s[10:11]
	v_lshlrev_b32_e32 v8, 3, v40
	v_lshlrev_b32_e32 v9, 3, v36
	v_mov_b32_dpp v16, v4 quad_perm:[1,0,3,2] row_mask:0xf bank_mask:0xf
	v_mov_b32_dpp v17, v5 quad_perm:[1,0,3,2] row_mask:0xf bank_mask:0xf
	v_add_u32_e32 v9, -8, v9
	v_cndmask_b32_e64 v44, v22, v16, s[10:11]
	v_cndmask_b32_e64 v45, v23, v17, s[10:11]
	v_cndmask_b32_e64 v46, v16, v10, s[10:11]
	v_cndmask_b32_e64 v47, v17, v11, s[10:11]
	v_cndmask_b32_e64 v8, v8, v9, s[10:11]
	global_store_dwordx4 v8, v[44:47], s[4:5] sc1
	s_and_saveexec_b64 s[6:7], vcc
	s_cbranch_execz .LBB0_58
	v_mov_b32_e32 v43, 0
	v_cvt_pk_f16_f32 v3, v28, v29
	v_cvt_pk_f16_f32 v2, v26, v27
	v_lshl_add_u64 v[4:5], v[42:43], 3, s[4:5]
	global_store_dwordx2 v[4:5], v[2:3], off sc1

	.amdhsa_kernel _Z6k_partPKiPKfS2_S2_S2_S2_PiS3_PDF16_S4_S4_
		.amdhsa_group_segment_fixed_size 20544
		.amdhsa_private_segment_fixed_size 0
		.amdhsa_kernarg_size 88
		.amdhsa_user_sgpr_count 2
		.amdhsa_user_sgpr_dispatch_ptr 0
		.amdhsa_user_sgpr_queue_ptr 0
		.amdhsa_user_sgpr_kernarg_segment_ptr 1
		.amdhsa_user_sgpr_dispatch_id 0
		.amdhsa_user_sgpr_kernarg_preload_length 0
		.amdhsa_user_sgpr_kernarg_preload_offset 0
		.amdhsa_user_sgpr_private_segment_size 0
		.amdhsa_uses_dynamic_stack 0
		.amdhsa_enable_private_segment 0
		.amdhsa_system_sgpr_workgroup_id_x 1
		.amdhsa_system_sgpr_workgroup_id_y 0
		.amdhsa_system_sgpr_workgroup_id_z 0
		.amdhsa_system_sgpr_workgroup_info 0
		.amdhsa_system_vgpr_workitem_id 0
		.amdhsa_next_free_vgpr 48
		.amdhsa_next_free_sgpr 22
		.amdhsa_accum_offset 48
		.amdhsa_reserve_vcc 1
		.amdhsa_float_round_mode_32 0
		.amdhsa_float_round_mode_16_64 0
		.amdhsa_float_denorm_mode_32 3
		.amdhsa_float_denorm_mode_16_64 3
		.amdhsa_dx10_clamp 1
		.amdhsa_ieee_mode 1
		.amdhsa_fp16_overflow 0
		.amdhsa_tg_split 0
		.amdhsa_exception_fp_ieee_invalid_op 0
		.amdhsa_exception_fp_denorm_src 0
		.amdhsa_exception_fp_ieee_div_zero 0
		.amdhsa_exception_fp_ieee_overflow 0
		.amdhsa_exception_fp_ieee_underflow 0
		.amdhsa_exception_fp_ieee_inexact 0
		.amdhsa_exception_int_div_zero 0
	.end_amdhsa_kernel

amdhsa.kernels:
  - .agpr_count:     0
    .args:
      - .actual_access:  read_only
        .address_space:  global
        .offset:         0
        .size:           8
        .value_kind:     global_buffer
      - .actual_access:  read_only
        .address_space:  global
        .offset:         8
        .size:           8
        .value_kind:     global_buffer
      - .actual_access:  read_only
        .address_space:  global
        .offset:         16
        .size:           8
        .value_kind:     global_buffer
      - .actual_access:  read_only
        .address_space:  global
        .offset:         24
        .size:           8
        .value_kind:     global_buffer
      - .actual_access:  read_only
        .address_space:  global
        .offset:         32
        .size:           8
        .value_kind:     global_buffer
      - .actual_access:  read_only
        .address_space:  global
        .offset:         40
        .size:           8
        .value_kind:     global_buffer
      - .actual_access:  write_only
        .address_space:  global
        .offset:         48
        .size:           8
        .value_kind:     global_buffer
      - .actual_access:  write_only
        .address_space:  global
        .offset:         56
        .size:           8
        .value_kind:     global_buffer
      - .actual_access:  write_only
        .address_space:  global
        .offset:         64
        .size:           8
        .value_kind:     global_buffer
      - .actual_access:  write_only
        .address_space:  global
        .offset:         72
        .size:           8
        .value_kind:     global_buffer
      - .actual_access:  write_only
        .address_space:  global
        .offset:         80
        .size:           8
        .value_kind:     global_buffer
    .group_segment_fixed_size: 20544
    .kernarg_segment_align: 8
    .kernarg_segment_size: 88
    .language:       OpenCL C
    .language_version:
      - 2
      - 0
    .max_flat_workgroup_size: 1024
    .name:           _Z6k_partPKiPKfS2_S2_S2_S2_PiS3_PDF16_S4_S4_
    .private_segment_fixed_size: 0
    .sgpr_count:     28
    .sgpr_spill_count: 0
    .symbol:         _Z6k_partPKiPKfS2_S2_S2_S2_PiS3_PDF16_S4_S4_.kd
    .uniform_work_group_size: 1
    .uses_dynamic_stack: false
    .vgpr_count:     48
    .vgpr_spill_count: 0
    .wavefront_size: 64
  - .agpr_count:     0
    .args:
      - .actual_access:  read_only
        .address_space:  global
        .offset:         0
        .size:           8
        .value_kind:     global_buffer
      - .actual_access:  read_only
        .address_space:  global
        .offset:         8
        .size:           8
        .value_kind:     global_buffer
      - .actual_access:  read_only
        .address_space:  global
        .offset:         16
        .size:           8
        .value_kind:     global_buffer
      - .actual_access:  write_only
        .address_space:  global
        .offset:         24
        .size:           8
        .value_kind:     global_buffer
      - .address_space:  global
        .offset:         32
        .size:           8
        .value_kind:     global_buffer
      - .actual_access:  read_only
        .address_space:  global
        .offset:         40
        .size:           8
        .value_kind:     global_buffer
      - .actual_access:  read_only
        .address_space:  global
        .offset:         48
        .size:           8
        .value_kind:     global_buffer
      - .actual_access:  read_only
        .address_space:  global
        .offset:         56
        .size:           8
        .value_kind:     global_buffer
      - .actual_access:  read_only
        .address_space:  global
        .offset:         64
        .size:           8
        .value_kind:     global_buffer
      - .actual_access:  write_only
        .address_space:  global
        .offset:         72
        .size:           8
        .value_kind:     global_buffer
      - .actual_access:  write_only
        .address_space:  global
        .offset:         80
        .size:           8
        .value_kind:     global_buffer
    .group_segment_fixed_size: 38832
    .kernarg_segment_align: 8
    .kernarg_segment_size: 88
    .language:       OpenCL C
    .language_version:
      - 2
      - 0
    .max_flat_workgroup_size: 512
    .name:           _Z8k_layer1PKDF16_PKiS2_PiS3_PKDv4_jS6_PKfS8_P15HIP_vector_typeIfLj2EESB_
    .private_segment_fixed_size: 0
    .sgpr_count:     76
    .sgpr_spill_count: 0
    .symbol:         _Z8k_layer1PKDF16_PKiS2_PiS3_PKDv4_jS6_PKfS8_P15HIP_vector_typeIfLj2EESB_.kd
    .uniform_work_group_size: 1
    .uses_dynamic_stack: false
    .vgpr_count:     64
    .vgpr_spill_count: 0
    .wavefront_size: 64
  - .agpr_count:     0
    .args:
      - .actual_access:  read_only
        .address_space:  global
        .offset:         0
        .size:           8
        .value_kind:     global_buffer
      - .actual_access:  read_only
        .address_space:  global
        .offset:         8
        .size:           8
        .value_kind:     global_buffer
      - .actual_access:  read_only
        .address_space:  global
        .offset:         16
        .size:           8
        .value_kind:     global_buffer
      - .actual_access:  read_only
        .address_space:  global
        .offset:         24
        .size:           8
        .value_kind:     global_buffer
      - .actual_access:  write_only
        .address_space:  global
        .offset:         32
        .size:           8
        .value_kind:     global_buffer
    .group_segment_fixed_size: 0
    .kernarg_segment_align: 8
    .kernarg_segment_size: 40
    .language:       OpenCL C
    .language_version:
      - 2
      - 0
    .max_flat_workgroup_size: 448
    .name:           _Z8k_layer2PK15HIP_vector_typeIfLj2EES2_PKiS4_PS0_
    .private_segment_fixed_size: 0
    .sgpr_count:     21
    .sgpr_spill_count: 0
    .symbol:         _Z8k_layer2PK15HIP_vector_typeIfLj2EES2_PKiS4_PS0_.kd
    .uniform_work_group_size: 1
    .uses_dynamic_stack: false
    .vgpr_count:     25
    .vgpr_spill_count: 0
    .wavefront_size: 64
